# sel: the third block's next-triple DMA is issued at the second block's head (spread 1,2,0) so the last pieces get more time to land before the triple barrier
# baseline (speedup 1.0000x reference)
; #define LAS __attribute__((address_space(3)))
; __device__ __forceinline__ void ringS_dma(const RingSLane& R, const char* K8p, const char* VTp, LAS unsigned char* sb, int wave) {
;     __builtin_amdgcn_global_load_lds((const unsigned*)(K8p + R.so[0]), (LAS unsigned*)(sb + wave * 1024), 16, 0, 0);
;     __builtin_amdgcn_global_load_lds((const unsigned*)((wave == 0 ? K8p : VTp) + R.so[1]), (LAS unsigned*)(sb + (wave + 8) * 1024), 16, 0, 0);
;     if (wave <= 2) __builtin_amdgcn_global_load_lds((const unsigned*)(VTp + R.so[2]), (LAS unsigned*)(sb + (wave + 16) * 1024), 16, 0, 0);
; }
.Lsel_dma2chk:
	s_cmp_eq_u32 s37, 1
	s_cbranch_scc0 .Lsel_nodma
	s_bitcmp1_b32 s99, 2
	s_cbranch_scc0 .Lsel_nodma
	s_lshr_b32 s12, s60, 16
	s_and_b32 s12, s12, 0xff
	s_lshl_b32 s12, s12, 13
	s_add_u32 s44, s62, s12
	s_addc_u32 s45, s63, 0
	s_add_u32 s12, s64, s12
	s_addc_u32 s13, s65, 0
	s_add_i32 s97, s98, 0x9800
	s_mov_b32 m0, s97
	s_and_b64 vcc, exec, s[16:17]
	global_load_lds_dwordx4 v102, s[44:45]
	s_cselect_b32 s45, s45, s13
	s_cselect_b32 s44, s44, s12
	s_add_i32 m0, s97, 0x2000
	s_and_b64 vcc, exec, s[10:11]
	global_load_lds_dwordx4 v106, s[44:45]
	s_cbranch_vccnz .Lsel_dma2done
	s_add_i32 m0, s97, 0x4000
	s_nop 0
	global_load_lds_dwordx4 v108, s[12:13]
.Lsel_dma2done:
	s_bitset0_b32 s99, 2
